# GEMM2 epilogue: residual base loads hoisted into batches (2 exposed latencies per unit instead of 16)
# speedup vs baseline: 1.0057x; 1.0057x over previous
.LBB0_1484:
	v_lshl_add_u32 v146, s10, 8, v1
	v_lshl_or_b32 v144, s24, 8, v161
	v_ashrrev_i32_e32 v147, 31, v146
	v_ashrrev_i32_e32 v145, 31, v144
	v_lshlrev_b64 v[148:149], 11, v[146:147]
	v_lshl_add_u64 v[148:149], v[148:149], 0, v[144:145]
	v_cndmask_b32_e64 v150, 0, 1, s[8:9]
	v_cmp_ne_u32_e64 s[10:11], 1, v150
	s_andn2_b64 vcc, exec, s[8:9]
	v_lshl_add_u64 v[150:151], v[148:149], 2, v[138:139]
	s_cbranch_vccnz .LBB0_1535
	v_mov_b64_e32 v[236:237], v[150:151]
	v_mov_b64_e32 v[238:239], v[236:237]
	global_load_dwordx4 v[166:169], v[238:239], off
	global_load_dwordx4 v[170:173], v[238:239], off offset:16
	global_load_dwordx4 v[174:177], v[238:239], off offset:512
	global_load_dwordx4 v[178:181], v[238:239], off offset:528
	v_add_co_u32_e32 v238, vcc, 0x20000, v236
	s_nop 1
	v_addc_co_u32_e32 v239, vcc, 0, v237, vcc
	global_load_dwordx4 v[182:185], v[238:239], off
	global_load_dwordx4 v[186:189], v[238:239], off offset:16
	global_load_dwordx4 v[190:193], v[238:239], off offset:512
	global_load_dwordx4 v[194:197], v[238:239], off offset:528
	v_add_co_u32_e32 v238, vcc, 0x40000, v236
	s_nop 1
	v_addc_co_u32_e32 v239, vcc, 0, v237, vcc
	global_load_dwordx4 v[198:201], v[238:239], off
	global_load_dwordx4 v[202:205], v[238:239], off offset:16
	global_load_dwordx4 v[206:209], v[238:239], off offset:512
	global_load_dwordx4 v[210:213], v[238:239], off offset:528
	v_add_co_u32_e32 v238, vcc, 0x60000, v236
	s_nop 1
	v_addc_co_u32_e32 v239, vcc, 0, v237, vcc
	global_load_dwordx4 v[214:217], v[238:239], off
	global_load_dwordx4 v[218:221], v[238:239], off offset:16
	global_load_dwordx4 v[222:225], v[238:239], off offset:512
	global_load_dwordx4 v[226:229], v[238:239], off offset:528
	s_waitcnt vmcnt(0)
	v_mov_b64_e32 v[152:153], v[166:167]
	v_mov_b64_e32 v[154:155], v[168:169]
	v_mov_b64_e32 v[156:157], v[170:171]
	v_mov_b64_e32 v[158:159], v[172:173]
	v_pk_add_f32 v[154:155], v[128:129], v[154:155]
	v_pk_add_f32 v[152:153], v[126:127], v[152:153]
	v_pk_add_f32 v[158:159], v[124:125], v[158:159]
	v_pk_add_f32 v[156:157], v[122:123], v[156:157]
	v_lshl_add_u64 v[148:149], v[148:149], 1, s[4:5]
	s_cbranch_execnz .LBB0_1487

.LBB0_1487:
	s_and_b64 vcc, exec, s[10:11]
	v_cvt_pk_bf16_f32 v122, v152, v153
	v_cvt_pk_bf16_f32 v123, v154, v155
	v_cvt_pk_bf16_f32 v124, v156, v157
	v_cvt_pk_bf16_f32 v125, v158, v159
	global_store_dwordx4 v[148:149], v[122:125], off
	s_cbranch_vccnz .LBB0_1536
	s_nop 1
	v_mov_b64_e32 v[122:123], v[174:175]
	v_mov_b64_e32 v[124:125], v[176:177]
	v_mov_b64_e32 v[126:127], v[178:179]
	v_mov_b64_e32 v[128:129], v[180:181]
	v_pk_add_f32 v[124:125], v[120:121], v[124:125]
	v_pk_add_f32 v[122:123], v[118:119], v[122:123]
	v_pk_add_f32 v[128:129], v[116:117], v[128:129]
	v_pk_add_f32 v[126:127], v[114:115], v[126:127]
	s_cbranch_execnz .LBB0_1490

.LBB0_1490:
	v_cvt_pk_bf16_f32 v114, v122, v123
	v_cvt_pk_bf16_f32 v115, v124, v125
	v_cvt_pk_bf16_f32 v116, v126, v127
	s_nop 0
	v_cvt_pk_bf16_f32 v117, v128, v129
	global_store_dwordx4 v[148:149], v[114:117], off offset:256
	s_and_b64 vcc, exec, s[10:11]
	s_nop 0
	v_or_b32_e32 v114, 16, v146
	v_ashrrev_i32_e32 v115, 31, v114
	v_lshlrev_b64 v[114:115], 11, v[114:115]
	v_lshl_add_u64 v[114:115], v[114:115], 0, v[144:145]
	v_lshl_add_u64 v[116:117], v[114:115], 2, v[138:139]
	s_cbranch_vccnz .LBB0_1537
	v_mov_b64_e32 v[118:119], v[182:183]
	v_mov_b64_e32 v[120:121], v[184:185]
	v_mov_b64_e32 v[122:123], v[186:187]
	v_mov_b64_e32 v[124:125], v[188:189]
	v_pk_add_f32 v[120:121], v[112:113], v[120:121]
	v_pk_add_f32 v[118:119], v[110:111], v[118:119]
	v_pk_add_f32 v[124:125], v[108:109], v[124:125]
	v_pk_add_f32 v[122:123], v[106:107], v[122:123]
	v_lshl_add_u64 v[114:115], v[114:115], 1, s[4:5]
	s_cbranch_execnz .LBB0_1493

.LBB0_1493:
	s_and_b64 vcc, exec, s[10:11]
	v_cvt_pk_bf16_f32 v106, v118, v119
	v_cvt_pk_bf16_f32 v107, v120, v121
	v_cvt_pk_bf16_f32 v108, v122, v123
	v_cvt_pk_bf16_f32 v109, v124, v125
	global_store_dwordx4 v[114:115], v[106:109], off
	s_cbranch_vccnz .LBB0_1538
	s_nop 1
	v_mov_b64_e32 v[106:107], v[190:191]
	v_mov_b64_e32 v[108:109], v[192:193]
	v_mov_b64_e32 v[110:111], v[194:195]
	v_mov_b64_e32 v[112:113], v[196:197]
	v_pk_add_f32 v[108:109], v[104:105], v[108:109]
	v_pk_add_f32 v[106:107], v[102:103], v[106:107]
	v_pk_add_f32 v[112:113], v[100:101], v[112:113]
	v_pk_add_f32 v[110:111], v[98:99], v[110:111]
	s_cbranch_execnz .LBB0_1496

.LBB0_1496:
	v_cvt_pk_bf16_f32 v98, v106, v107
	v_cvt_pk_bf16_f32 v99, v108, v109
	v_cvt_pk_bf16_f32 v100, v110, v111
	s_nop 0
	v_cvt_pk_bf16_f32 v101, v112, v113
	global_store_dwordx4 v[114:115], v[98:101], off offset:256
	s_and_b64 vcc, exec, s[10:11]
	s_nop 0
	v_or_b32_e32 v98, 32, v146
	v_ashrrev_i32_e32 v99, 31, v98
	v_lshlrev_b64 v[98:99], 11, v[98:99]
	v_lshl_add_u64 v[98:99], v[98:99], 0, v[144:145]
	v_lshl_add_u64 v[100:101], v[98:99], 2, v[138:139]
	s_cbranch_vccnz .LBB0_1539
	v_mov_b64_e32 v[102:103], v[198:199]
	v_mov_b64_e32 v[104:105], v[200:201]
	v_mov_b64_e32 v[106:107], v[202:203]
	v_mov_b64_e32 v[108:109], v[204:205]
	v_pk_add_f32 v[104:105], v[96:97], v[104:105]
	v_pk_add_f32 v[102:103], v[94:95], v[102:103]
	v_pk_add_f32 v[108:109], v[92:93], v[108:109]
	v_pk_add_f32 v[106:107], v[90:91], v[106:107]
	v_lshl_add_u64 v[98:99], v[98:99], 1, s[4:5]
	s_cbranch_execnz .LBB0_1499

.LBB0_1499:
	s_and_b64 vcc, exec, s[10:11]
	v_cvt_pk_bf16_f32 v90, v102, v103
	v_cvt_pk_bf16_f32 v91, v104, v105
	v_cvt_pk_bf16_f32 v92, v106, v107
	v_cvt_pk_bf16_f32 v93, v108, v109
	global_store_dwordx4 v[98:99], v[90:93], off
	s_cbranch_vccnz .LBB0_1540
	s_nop 1
	v_mov_b64_e32 v[90:91], v[206:207]
	v_mov_b64_e32 v[92:93], v[208:209]
	v_mov_b64_e32 v[94:95], v[210:211]
	v_mov_b64_e32 v[96:97], v[212:213]
	v_pk_add_f32 v[92:93], v[88:89], v[92:93]
	v_pk_add_f32 v[90:91], v[86:87], v[90:91]
	v_pk_add_f32 v[96:97], v[84:85], v[96:97]
	v_pk_add_f32 v[94:95], v[82:83], v[94:95]
	s_cbranch_execnz .LBB0_1502

.LBB0_1502:
	v_cvt_pk_bf16_f32 v82, v90, v91
	v_cvt_pk_bf16_f32 v83, v92, v93
	v_cvt_pk_bf16_f32 v84, v94, v95
	s_nop 0
	v_cvt_pk_bf16_f32 v85, v96, v97
	global_store_dwordx4 v[98:99], v[82:85], off offset:256
	s_and_b64 vcc, exec, s[10:11]
	s_nop 0
	v_or_b32_e32 v82, 48, v146
	v_ashrrev_i32_e32 v83, 31, v82
	v_lshlrev_b64 v[82:83], 11, v[82:83]
	v_lshl_add_u64 v[82:83], v[82:83], 0, v[144:145]
	v_lshl_add_u64 v[84:85], v[82:83], 2, v[138:139]
	s_cbranch_vccnz .LBB0_1541
	v_mov_b64_e32 v[86:87], v[214:215]
	v_mov_b64_e32 v[88:89], v[216:217]
	v_mov_b64_e32 v[90:91], v[218:219]
	v_mov_b64_e32 v[92:93], v[220:221]
	v_pk_add_f32 v[88:89], v[80:81], v[88:89]
	v_pk_add_f32 v[86:87], v[78:79], v[86:87]
	v_pk_add_f32 v[92:93], v[76:77], v[92:93]
	v_pk_add_f32 v[90:91], v[74:75], v[90:91]
	v_lshl_add_u64 v[82:83], v[82:83], 1, s[4:5]
	s_cbranch_execnz .LBB0_1505

.LBB0_1505:
	s_and_b64 vcc, exec, s[10:11]
	v_cvt_pk_bf16_f32 v74, v86, v87
	v_cvt_pk_bf16_f32 v75, v88, v89
	v_cvt_pk_bf16_f32 v76, v90, v91
	v_cvt_pk_bf16_f32 v77, v92, v93
	global_store_dwordx4 v[82:83], v[74:77], off
	s_cbranch_vccnz .LBB0_1542
	s_nop 1
	v_mov_b64_e32 v[74:75], v[222:223]
	v_mov_b64_e32 v[76:77], v[224:225]
	v_mov_b64_e32 v[78:79], v[226:227]
	v_mov_b64_e32 v[80:81], v[228:229]
	v_pk_add_f32 v[76:77], v[72:73], v[76:77]
	v_pk_add_f32 v[74:75], v[70:71], v[74:75]
	v_pk_add_f32 v[80:81], v[68:69], v[80:81]
	v_pk_add_f32 v[78:79], v[66:67], v[78:79]
	s_cbranch_execnz .LBB0_1508

.LBB0_1508:
	v_cvt_pk_bf16_f32 v66, v74, v75
	v_cvt_pk_bf16_f32 v67, v76, v77
	v_cvt_pk_bf16_f32 v68, v78, v79
	s_nop 0
	v_cvt_pk_bf16_f32 v69, v80, v81
	global_store_dwordx4 v[82:83], v[66:69], off offset:256
	s_mov_b64 s[2:3], 0x40000
	s_and_b64 vcc, exec, s[10:11]
	v_lshlrev_b64 v[66:67], 11, v[146:147]
	v_lshl_add_u64 v[66:67], v[66:67], 0, v[144:145]
	v_lshl_add_u64 v[66:67], v[66:67], 0, s[2:3]
	v_lshl_add_u64 v[68:69], v[66:67], 2, v[138:139]
	s_cbranch_vccnz .LBB0_1543
	v_add_co_u32_e32 v238, vcc, 0x100000, v236
	s_nop 1
	v_addc_co_u32_e32 v239, vcc, 0, v237, vcc
	global_load_dwordx4 v[166:169], v[238:239], off
	global_load_dwordx4 v[170:173], v[238:239], off offset:16
	global_load_dwordx4 v[174:177], v[238:239], off offset:512
	global_load_dwordx4 v[178:181], v[238:239], off offset:528
	v_add_co_u32_e32 v238, vcc, 0x120000, v236
	s_nop 1
	v_addc_co_u32_e32 v239, vcc, 0, v237, vcc
	global_load_dwordx4 v[182:185], v[238:239], off
	global_load_dwordx4 v[186:189], v[238:239], off offset:16
	global_load_dwordx4 v[190:193], v[238:239], off offset:512
	global_load_dwordx4 v[194:197], v[238:239], off offset:528
	v_add_co_u32_e32 v238, vcc, 0x140000, v236
	s_nop 1
	v_addc_co_u32_e32 v239, vcc, 0, v237, vcc
	global_load_dwordx4 v[198:201], v[238:239], off
	global_load_dwordx4 v[202:205], v[238:239], off offset:16
	global_load_dwordx4 v[206:209], v[238:239], off offset:512
	global_load_dwordx4 v[210:213], v[238:239], off offset:528
	v_add_co_u32_e32 v238, vcc, 0x160000, v236
	s_nop 1
	v_addc_co_u32_e32 v239, vcc, 0, v237, vcc
	global_load_dwordx4 v[214:217], v[238:239], off
	global_load_dwordx4 v[218:221], v[238:239], off offset:16
	global_load_dwordx4 v[222:225], v[238:239], off offset:512
	global_load_dwordx4 v[226:229], v[238:239], off offset:528
	s_waitcnt vmcnt(0)
	v_mov_b64_e32 v[70:71], v[166:167]
	v_mov_b64_e32 v[72:73], v[168:169]
	v_mov_b64_e32 v[74:75], v[170:171]
	v_mov_b64_e32 v[76:77], v[172:173]
	v_pk_add_f32 v[72:73], v[64:65], v[72:73]
	v_pk_add_f32 v[70:71], v[62:63], v[70:71]
	v_pk_add_f32 v[76:77], v[60:61], v[76:77]
	v_pk_add_f32 v[74:75], v[58:59], v[74:75]
	v_lshl_add_u64 v[66:67], v[66:67], 1, s[4:5]
	s_cbranch_execnz .LBB0_1511

.LBB0_1511:
	s_and_b64 vcc, exec, s[10:11]
	v_cvt_pk_bf16_f32 v58, v70, v71
	v_cvt_pk_bf16_f32 v59, v72, v73
	v_cvt_pk_bf16_f32 v60, v74, v75
	v_cvt_pk_bf16_f32 v61, v76, v77
	global_store_dwordx4 v[66:67], v[58:61], off
	s_cbranch_vccnz .LBB0_1544
	s_nop 1
	v_mov_b64_e32 v[58:59], v[174:175]
	v_mov_b64_e32 v[60:61], v[176:177]
	v_mov_b64_e32 v[62:63], v[178:179]
	v_mov_b64_e32 v[64:65], v[180:181]
	v_pk_add_f32 v[60:61], v[56:57], v[60:61]
	v_pk_add_f32 v[58:59], v[54:55], v[58:59]
	v_pk_add_f32 v[64:65], v[52:53], v[64:65]
	v_pk_add_f32 v[62:63], v[50:51], v[62:63]
	s_cbranch_execnz .LBB0_1514

.LBB0_1514:
	v_cvt_pk_bf16_f32 v50, v58, v59
	v_cvt_pk_bf16_f32 v51, v60, v61
	v_cvt_pk_bf16_f32 v52, v62, v63
	s_nop 0
	v_cvt_pk_bf16_f32 v53, v64, v65
	global_store_dwordx4 v[66:67], v[50:53], off offset:256
	s_mov_b64 s[2:3], 0x48000
	s_and_b64 vcc, exec, s[10:11]
	v_lshlrev_b64 v[50:51], 11, v[146:147]
	v_lshl_add_u64 v[50:51], v[50:51], 0, v[144:145]
	v_lshl_add_u64 v[50:51], v[50:51], 0, s[2:3]
	v_lshl_add_u64 v[52:53], v[50:51], 2, v[138:139]
	s_cbranch_vccnz .LBB0_1545
	v_mov_b64_e32 v[54:55], v[182:183]
	v_mov_b64_e32 v[56:57], v[184:185]
	v_mov_b64_e32 v[58:59], v[186:187]
	v_mov_b64_e32 v[60:61], v[188:189]
	v_pk_add_f32 v[56:57], v[48:49], v[56:57]
	v_pk_add_f32 v[54:55], v[46:47], v[54:55]
	v_pk_add_f32 v[60:61], v[44:45], v[60:61]
	v_pk_add_f32 v[58:59], v[42:43], v[58:59]
	v_lshl_add_u64 v[50:51], v[50:51], 1, s[4:5]
	s_cbranch_execnz .LBB0_1517

.LBB0_1517:
	s_and_b64 vcc, exec, s[10:11]
	v_cvt_pk_bf16_f32 v42, v54, v55
	v_cvt_pk_bf16_f32 v43, v56, v57
	v_cvt_pk_bf16_f32 v44, v58, v59
	v_cvt_pk_bf16_f32 v45, v60, v61
	global_store_dwordx4 v[50:51], v[42:45], off
	s_cbranch_vccnz .LBB0_1546
	s_nop 1
	v_mov_b64_e32 v[42:43], v[190:191]
	v_mov_b64_e32 v[44:45], v[192:193]
	v_mov_b64_e32 v[46:47], v[194:195]
	v_mov_b64_e32 v[48:49], v[196:197]
	v_pk_add_f32 v[44:45], v[40:41], v[44:45]
	v_pk_add_f32 v[42:43], v[38:39], v[42:43]
	v_pk_add_f32 v[48:49], v[36:37], v[48:49]
	v_pk_add_f32 v[46:47], v[34:35], v[46:47]
	s_cbranch_execnz .LBB0_1520

.LBB0_1520:
	v_cvt_pk_bf16_f32 v34, v42, v43
	v_cvt_pk_bf16_f32 v35, v44, v45
	v_cvt_pk_bf16_f32 v36, v46, v47
	s_nop 0
	v_cvt_pk_bf16_f32 v37, v48, v49
	global_store_dwordx4 v[50:51], v[34:37], off offset:256
	s_mov_b64 s[2:3], 0x50000
	s_and_b64 vcc, exec, s[10:11]
	v_lshlrev_b64 v[34:35], 11, v[146:147]
	v_lshl_add_u64 v[34:35], v[34:35], 0, v[144:145]
	v_lshl_add_u64 v[34:35], v[34:35], 0, s[2:3]
	v_lshl_add_u64 v[36:37], v[34:35], 2, v[138:139]
	s_cbranch_vccnz .LBB0_1547
	v_mov_b64_e32 v[38:39], v[198:199]
	v_mov_b64_e32 v[40:41], v[200:201]
	v_mov_b64_e32 v[42:43], v[202:203]
	v_mov_b64_e32 v[44:45], v[204:205]
	v_pk_add_f32 v[40:41], v[32:33], v[40:41]
	v_pk_add_f32 v[38:39], v[30:31], v[38:39]
	v_pk_add_f32 v[44:45], v[28:29], v[44:45]
	v_pk_add_f32 v[42:43], v[26:27], v[42:43]
	v_lshl_add_u64 v[34:35], v[34:35], 1, s[4:5]
	s_cbranch_execnz .LBB0_1523

.LBB0_1523:
	s_and_b64 vcc, exec, s[10:11]
	v_cvt_pk_bf16_f32 v26, v38, v39
	v_cvt_pk_bf16_f32 v27, v40, v41
	v_cvt_pk_bf16_f32 v28, v42, v43
	v_cvt_pk_bf16_f32 v29, v44, v45
	global_store_dwordx4 v[34:35], v[26:29], off
	s_cbranch_vccnz .LBB0_1548
	s_nop 1
	v_mov_b64_e32 v[26:27], v[206:207]
	v_mov_b64_e32 v[28:29], v[208:209]
	v_mov_b64_e32 v[30:31], v[210:211]
	v_mov_b64_e32 v[32:33], v[212:213]
	v_pk_add_f32 v[28:29], v[24:25], v[28:29]
	v_pk_add_f32 v[26:27], v[22:23], v[26:27]
	v_pk_add_f32 v[32:33], v[20:21], v[32:33]
	v_pk_add_f32 v[30:31], v[18:19], v[30:31]
	s_cbranch_execnz .LBB0_1526

.LBB0_1526:
	v_cvt_pk_bf16_f32 v18, v26, v27
	v_cvt_pk_bf16_f32 v19, v28, v29
	v_cvt_pk_bf16_f32 v20, v30, v31
	s_nop 0
	v_cvt_pk_bf16_f32 v21, v32, v33
	global_store_dwordx4 v[34:35], v[18:21], off offset:256
	s_mov_b64 s[2:3], 0x58000
	s_and_b64 vcc, exec, s[10:11]
	v_lshlrev_b64 v[18:19], 11, v[146:147]
	v_lshl_add_u64 v[18:19], v[18:19], 0, v[144:145]
	v_lshl_add_u64 v[18:19], v[18:19], 0, s[2:3]
	v_lshl_add_u64 v[20:21], v[18:19], 2, v[138:139]
	s_cbranch_vccnz .LBB0_1549
	v_mov_b64_e32 v[22:23], v[214:215]
	v_mov_b64_e32 v[24:25], v[216:217]
	v_mov_b64_e32 v[26:27], v[218:219]
	v_mov_b64_e32 v[28:29], v[220:221]
	v_pk_add_f32 v[24:25], v[16:17], v[24:25]
	v_pk_add_f32 v[22:23], v[14:15], v[22:23]
	v_pk_add_f32 v[28:29], v[12:13], v[28:29]
	v_pk_add_f32 v[26:27], v[10:11], v[26:27]
	v_lshl_add_u64 v[18:19], v[18:19], 1, s[4:5]
	s_cbranch_execnz .LBB0_1529

.LBB0_1529:
	s_and_b64 vcc, exec, s[10:11]
	v_cvt_pk_bf16_f32 v10, v22, v23
	v_cvt_pk_bf16_f32 v11, v24, v25
	v_cvt_pk_bf16_f32 v12, v26, v27
	v_cvt_pk_bf16_f32 v13, v28, v29
	global_store_dwordx4 v[18:19], v[10:13], off
	s_cbranch_vccnz .LBB0_1550
	s_nop 1
	v_mov_b64_e32 v[10:11], v[222:223]
	v_mov_b64_e32 v[12:13], v[224:225]
	v_mov_b64_e32 v[14:15], v[226:227]
	v_mov_b64_e32 v[16:17], v[228:229]
	v_pk_add_f32 v[12:13], v[8:9], v[12:13]
	v_pk_add_f32 v[10:11], v[6:7], v[10:11]
	v_pk_add_f32 v[16:17], v[4:5], v[16:17]
	v_pk_add_f32 v[14:15], v[2:3], v[14:15]
	s_cbranch_execnz .LBB0_1532

.LBB0_3804:
	v_mov_b64_e32 v[152:153], v[166:167]
	v_mov_b64_e32 v[154:155], v[168:169]
	v_lshlrev_b32_e32 v156, 16, v152
	v_and_b32_e32 v157, 0xffff0000, v152
	v_lshlrev_b32_e32 v152, 16, v153
	v_and_b32_e32 v153, 0xffff0000, v153
	v_lshlrev_b32_e32 v158, 16, v154
	v_and_b32_e32 v159, 0xffff0000, v154
	v_lshlrev_b32_e32 v166, 16, v155
	v_and_b32_e32 v167, 0xffff0000, v155
	v_pk_add_f32 v[154:155], v[126:127], v[156:157]
	v_pk_add_f32 v[152:153], v[128:129], v[152:153]
	v_pk_add_f32 v[156:157], v[122:123], v[158:159]
	v_pk_add_f32 v[158:159], v[124:125], v[166:167]

.LBB0_3807:
	v_mov_b64_e32 v[122:123], v[170:171]
	v_mov_b64_e32 v[124:125], v[172:173]
	v_lshlrev_b32_e32 v126, 16, v122
	v_and_b32_e32 v127, 0xffff0000, v122
	v_lshlrev_b32_e32 v122, 16, v123
	v_and_b32_e32 v123, 0xffff0000, v123
	v_lshlrev_b32_e32 v128, 16, v124
	v_and_b32_e32 v129, 0xffff0000, v124
	v_lshlrev_b32_e32 v150, 16, v125
	v_and_b32_e32 v151, 0xffff0000, v125
	v_pk_add_f32 v[124:125], v[118:119], v[126:127]
	v_pk_add_f32 v[122:123], v[120:121], v[122:123]
	v_pk_add_f32 v[126:127], v[114:115], v[128:129]
	v_pk_add_f32 v[128:129], v[116:117], v[150:151]

.LBB0_3810:
	v_mov_b64_e32 v[118:119], v[174:175]
	v_mov_b64_e32 v[120:121], v[176:177]
	v_lshlrev_b32_e32 v122, 16, v118
	v_and_b32_e32 v123, 0xffff0000, v118
	v_lshlrev_b32_e32 v118, 16, v119
	v_and_b32_e32 v119, 0xffff0000, v119
	v_lshlrev_b32_e32 v124, 16, v120
	v_and_b32_e32 v125, 0xffff0000, v120
	v_lshlrev_b32_e32 v126, 16, v121
	v_and_b32_e32 v127, 0xffff0000, v121
	v_pk_add_f32 v[120:121], v[110:111], v[122:123]
	v_pk_add_f32 v[118:119], v[112:113], v[118:119]
	v_pk_add_f32 v[122:123], v[106:107], v[124:125]
	v_pk_add_f32 v[124:125], v[108:109], v[126:127]

.LBB0_3813:
	v_mov_b64_e32 v[106:107], v[178:179]
	v_mov_b64_e32 v[108:109], v[180:181]
	v_lshlrev_b32_e32 v110, 16, v106
	v_and_b32_e32 v111, 0xffff0000, v106
	v_lshlrev_b32_e32 v106, 16, v107
	v_and_b32_e32 v107, 0xffff0000, v107
	v_lshlrev_b32_e32 v112, 16, v108
	v_and_b32_e32 v113, 0xffff0000, v108
	v_lshlrev_b32_e32 v116, 16, v109
	v_and_b32_e32 v117, 0xffff0000, v109
	v_pk_add_f32 v[108:109], v[102:103], v[110:111]
	v_pk_add_f32 v[106:107], v[104:105], v[106:107]
	v_pk_add_f32 v[110:111], v[98:99], v[112:113]
	v_pk_add_f32 v[112:113], v[100:101], v[116:117]

.LBB0_3816:
	v_mov_b64_e32 v[102:103], v[182:183]
	v_mov_b64_e32 v[104:105], v[184:185]
	v_lshlrev_b32_e32 v106, 16, v102
	v_and_b32_e32 v107, 0xffff0000, v102
	v_lshlrev_b32_e32 v102, 16, v103
	v_and_b32_e32 v103, 0xffff0000, v103
	v_lshlrev_b32_e32 v108, 16, v104
	v_and_b32_e32 v109, 0xffff0000, v104
	v_lshlrev_b32_e32 v110, 16, v105
	v_and_b32_e32 v111, 0xffff0000, v105
	v_pk_add_f32 v[104:105], v[94:95], v[106:107]
	v_pk_add_f32 v[102:103], v[96:97], v[102:103]
	v_pk_add_f32 v[106:107], v[90:91], v[108:109]
	v_pk_add_f32 v[108:109], v[92:93], v[110:111]

.LBB0_3819:
	v_mov_b64_e32 v[90:91], v[186:187]
	v_mov_b64_e32 v[92:93], v[188:189]
	v_lshlrev_b32_e32 v94, 16, v90
	v_and_b32_e32 v95, 0xffff0000, v90
	v_lshlrev_b32_e32 v90, 16, v91
	v_and_b32_e32 v91, 0xffff0000, v91
	v_lshlrev_b32_e32 v96, 16, v92
	v_and_b32_e32 v97, 0xffff0000, v92
	v_lshlrev_b32_e32 v100, 16, v93
	v_and_b32_e32 v101, 0xffff0000, v93
	v_pk_add_f32 v[92:93], v[86:87], v[94:95]
	v_pk_add_f32 v[90:91], v[88:89], v[90:91]
	v_pk_add_f32 v[94:95], v[82:83], v[96:97]
	v_pk_add_f32 v[96:97], v[84:85], v[100:101]

.LBB0_3822:
	v_mov_b64_e32 v[86:87], v[190:191]
	v_mov_b64_e32 v[88:89], v[192:193]
	v_lshlrev_b32_e32 v90, 16, v86
	v_and_b32_e32 v91, 0xffff0000, v86
	v_lshlrev_b32_e32 v86, 16, v87
	v_and_b32_e32 v87, 0xffff0000, v87
	v_lshlrev_b32_e32 v92, 16, v88
	v_and_b32_e32 v93, 0xffff0000, v88
	v_lshlrev_b32_e32 v94, 16, v89
	v_and_b32_e32 v95, 0xffff0000, v89
	v_pk_add_f32 v[88:89], v[78:79], v[90:91]
	v_pk_add_f32 v[86:87], v[80:81], v[86:87]
	v_pk_add_f32 v[90:91], v[74:75], v[92:93]
	v_pk_add_f32 v[92:93], v[76:77], v[94:95]

.LBB0_3825:
	v_mov_b64_e32 v[74:75], v[194:195]
	v_mov_b64_e32 v[76:77], v[196:197]
	v_lshlrev_b32_e32 v78, 16, v74
	v_and_b32_e32 v79, 0xffff0000, v74
	v_lshlrev_b32_e32 v74, 16, v75
	v_and_b32_e32 v75, 0xffff0000, v75
	v_lshlrev_b32_e32 v80, 16, v76
	v_and_b32_e32 v81, 0xffff0000, v76
	v_lshlrev_b32_e32 v84, 16, v77
	v_and_b32_e32 v85, 0xffff0000, v77
	v_pk_add_f32 v[76:77], v[70:71], v[78:79]
	v_pk_add_f32 v[74:75], v[72:73], v[74:75]
	v_pk_add_f32 v[78:79], v[66:67], v[80:81]
	v_pk_add_f32 v[80:81], v[68:69], v[84:85]

.LBB0_3828:
	v_mov_b64_e32 v[70:71], v[198:199]
	v_mov_b64_e32 v[72:73], v[200:201]
	v_lshlrev_b32_e32 v74, 16, v70
	v_and_b32_e32 v75, 0xffff0000, v70
	v_lshlrev_b32_e32 v70, 16, v71
	v_and_b32_e32 v71, 0xffff0000, v71
	v_lshlrev_b32_e32 v76, 16, v72
	v_and_b32_e32 v77, 0xffff0000, v72
	v_lshlrev_b32_e32 v78, 16, v73
	v_and_b32_e32 v79, 0xffff0000, v73
	v_pk_add_f32 v[72:73], v[62:63], v[74:75]
	v_pk_add_f32 v[70:71], v[64:65], v[70:71]
	v_pk_add_f32 v[74:75], v[58:59], v[76:77]
	v_pk_add_f32 v[76:77], v[60:61], v[78:79]

.LBB0_3831:
	v_mov_b64_e32 v[58:59], v[202:203]
	v_mov_b64_e32 v[60:61], v[204:205]
	v_lshlrev_b32_e32 v62, 16, v58
	v_and_b32_e32 v63, 0xffff0000, v58
	v_lshlrev_b32_e32 v58, 16, v59
	v_and_b32_e32 v59, 0xffff0000, v59
	v_lshlrev_b32_e32 v64, 16, v60
	v_and_b32_e32 v65, 0xffff0000, v60
	v_lshlrev_b32_e32 v68, 16, v61
	v_and_b32_e32 v69, 0xffff0000, v61
	v_pk_add_f32 v[60:61], v[54:55], v[62:63]
	v_pk_add_f32 v[58:59], v[56:57], v[58:59]
	v_pk_add_f32 v[62:63], v[50:51], v[64:65]
	v_pk_add_f32 v[64:65], v[52:53], v[68:69]

.LBB0_3834:
	v_mov_b64_e32 v[54:55], v[206:207]
	v_mov_b64_e32 v[56:57], v[208:209]
	v_lshlrev_b32_e32 v58, 16, v54
	v_and_b32_e32 v59, 0xffff0000, v54
	v_lshlrev_b32_e32 v54, 16, v55
	v_and_b32_e32 v55, 0xffff0000, v55
	v_lshlrev_b32_e32 v60, 16, v56
	v_and_b32_e32 v61, 0xffff0000, v56
	v_lshlrev_b32_e32 v62, 16, v57
	v_and_b32_e32 v63, 0xffff0000, v57
	v_pk_add_f32 v[56:57], v[46:47], v[58:59]
	v_pk_add_f32 v[54:55], v[48:49], v[54:55]
	v_pk_add_f32 v[58:59], v[42:43], v[60:61]
	v_pk_add_f32 v[60:61], v[44:45], v[62:63]

.LBB0_3837:
	v_mov_b64_e32 v[42:43], v[210:211]
	v_mov_b64_e32 v[44:45], v[212:213]
	v_lshlrev_b32_e32 v46, 16, v42
	v_and_b32_e32 v47, 0xffff0000, v42
	v_lshlrev_b32_e32 v42, 16, v43
	v_and_b32_e32 v43, 0xffff0000, v43
	v_lshlrev_b32_e32 v48, 16, v44
	v_and_b32_e32 v49, 0xffff0000, v44
	v_lshlrev_b32_e32 v52, 16, v45
	v_and_b32_e32 v53, 0xffff0000, v45
	v_pk_add_f32 v[44:45], v[38:39], v[46:47]
	v_pk_add_f32 v[42:43], v[40:41], v[42:43]
	v_pk_add_f32 v[46:47], v[34:35], v[48:49]
	v_pk_add_f32 v[48:49], v[36:37], v[52:53]

.LBB0_3840:
	v_mov_b64_e32 v[38:39], v[214:215]
	v_mov_b64_e32 v[40:41], v[216:217]
	v_lshlrev_b32_e32 v42, 16, v38
	v_and_b32_e32 v43, 0xffff0000, v38
	v_lshlrev_b32_e32 v38, 16, v39
	v_and_b32_e32 v39, 0xffff0000, v39
	v_lshlrev_b32_e32 v44, 16, v40
	v_and_b32_e32 v45, 0xffff0000, v40
	v_lshlrev_b32_e32 v46, 16, v41
	v_and_b32_e32 v47, 0xffff0000, v41
	v_pk_add_f32 v[40:41], v[30:31], v[42:43]
	v_pk_add_f32 v[38:39], v[32:33], v[38:39]
	v_pk_add_f32 v[42:43], v[26:27], v[44:45]
	v_pk_add_f32 v[44:45], v[28:29], v[46:47]

.LBB0_3843:
	v_mov_b64_e32 v[26:27], v[218:219]
	v_mov_b64_e32 v[28:29], v[220:221]
	v_lshlrev_b32_e32 v30, 16, v26
	v_and_b32_e32 v31, 0xffff0000, v26
	v_lshlrev_b32_e32 v26, 16, v27
	v_and_b32_e32 v27, 0xffff0000, v27
	v_lshlrev_b32_e32 v32, 16, v28
	v_and_b32_e32 v33, 0xffff0000, v28
	v_lshlrev_b32_e32 v36, 16, v29
	v_and_b32_e32 v37, 0xffff0000, v29
	v_pk_add_f32 v[28:29], v[22:23], v[30:31]
	v_pk_add_f32 v[26:27], v[24:25], v[26:27]
	v_pk_add_f32 v[30:31], v[18:19], v[32:33]
	v_pk_add_f32 v[32:33], v[20:21], v[36:37]

.LBB0_3846:
	v_mov_b64_e32 v[22:23], v[222:223]
	v_mov_b64_e32 v[24:25], v[224:225]
	v_lshlrev_b32_e32 v26, 16, v22
	v_and_b32_e32 v27, 0xffff0000, v22
	v_lshlrev_b32_e32 v22, 16, v23
	v_and_b32_e32 v23, 0xffff0000, v23
	v_lshlrev_b32_e32 v28, 16, v24
	v_and_b32_e32 v29, 0xffff0000, v24
	v_lshlrev_b32_e32 v30, 16, v25
	v_and_b32_e32 v31, 0xffff0000, v25
	v_pk_add_f32 v[24:25], v[14:15], v[26:27]
	v_pk_add_f32 v[22:23], v[16:17], v[22:23]
	v_pk_add_f32 v[26:27], v[10:11], v[28:29]
	v_pk_add_f32 v[28:29], v[12:13], v[30:31]

.LBB0_3849:
	v_mov_b64_e32 v[10:11], v[226:227]
	v_mov_b64_e32 v[12:13], v[228:229]
	v_lshlrev_b32_e32 v14, 16, v10
	v_and_b32_e32 v15, 0xffff0000, v10
	v_lshlrev_b32_e32 v10, 16, v11
	v_and_b32_e32 v11, 0xffff0000, v11
	v_lshlrev_b32_e32 v16, 16, v12
	v_and_b32_e32 v17, 0xffff0000, v12
	v_lshlrev_b32_e32 v20, 16, v13
	v_and_b32_e32 v21, 0xffff0000, v13
	v_pk_add_f32 v[12:13], v[6:7], v[14:15]
	v_pk_add_f32 v[10:11], v[8:9], v[10:11]
	v_pk_add_f32 v[14:15], v[2:3], v[16:17]
	v_pk_add_f32 v[16:17], v[4:5], v[20:21]

.LBB0_3853:
	v_lshl_add_u64 v[148:149], v[148:149], 1, s[12:13]
	v_mov_b64_e32 v[236:237], v[148:149]
	v_mov_b64_e32 v[238:239], v[236:237]
	global_load_dwordx4 v[166:169], v[238:239], off
	global_load_dwordx4 v[170:173], v[238:239], off offset:256
	v_add_co_u32_e32 v238, vcc, 0x10000, v236
	s_nop 1
	v_addc_co_u32_e32 v239, vcc, 0, v237, vcc
	global_load_dwordx4 v[174:177], v[238:239], off
	global_load_dwordx4 v[178:181], v[238:239], off offset:256
	v_add_co_u32_e32 v238, vcc, 0x20000, v236
	s_nop 1
	v_addc_co_u32_e32 v239, vcc, 0, v237, vcc
	global_load_dwordx4 v[182:185], v[238:239], off
	global_load_dwordx4 v[186:189], v[238:239], off offset:256
	v_add_co_u32_e32 v238, vcc, 0x30000, v236
	s_nop 1
	v_addc_co_u32_e32 v239, vcc, 0, v237, vcc
	global_load_dwordx4 v[190:193], v[238:239], off
	global_load_dwordx4 v[194:197], v[238:239], off offset:256
	v_add_co_u32_e32 v238, vcc, 0x80000, v236
	s_nop 1
	v_addc_co_u32_e32 v239, vcc, 0, v237, vcc
	global_load_dwordx4 v[198:201], v[238:239], off
	global_load_dwordx4 v[202:205], v[238:239], off offset:256
	v_add_co_u32_e32 v238, vcc, 0x90000, v236
	s_nop 1
	v_addc_co_u32_e32 v239, vcc, 0, v237, vcc
	global_load_dwordx4 v[206:209], v[238:239], off
	global_load_dwordx4 v[210:213], v[238:239], off offset:256
	v_add_co_u32_e32 v238, vcc, 0xa0000, v236
	s_nop 1
	v_addc_co_u32_e32 v239, vcc, 0, v237, vcc
	global_load_dwordx4 v[214:217], v[238:239], off
	global_load_dwordx4 v[218:221], v[238:239], off offset:256
	v_add_co_u32_e32 v238, vcc, 0xb0000, v236
	s_nop 1
	v_addc_co_u32_e32 v239, vcc, 0, v237, vcc
	global_load_dwordx4 v[222:225], v[238:239], off
	global_load_dwordx4 v[226:229], v[238:239], off offset:256
	s_waitcnt vmcnt(0)
	s_branch .LBB0_3804
